# cfgL + w_in1 (layer-1 input projection) weight conversion also moved from PRO into the H0-shadow converters
# baseline (speedup 1.0000x reference)
.LBB0_85:
	s_or_b64 exec, exec, s[0:1]
	s_movk_i32 s0, 0xa80
	v_cmp_gt_i32_e32 vcc, s0, v69
	s_cmp_eq_u32 s99, 1
	s_cselect_b64 vcc, vcc, 0
	s_and_saveexec_b64 s[0:1], vcc
	s_cbranch_execz .LBB0_120
	v_mov_b32_e32 v77, 0
	v_lshl_add_u64 v[2:3], s[58:59], 0, v[76:77]
	s_mov_b64 s[8:9], 0x3c300000
	v_lshl_or_b32 v77, s96, 9, v94
	v_lshl_add_u64 v[82:83], v[2:3], 0, s[8:9]
	v_or_b32_e32 v2, v77, v93
	s_movk_i32 s17, 0x1410
	s_lshl_b32 s16, s3, 6
	v_mul_lo_u32 v84, v2, s17
	s_mul_i32 s18, s3, 0x50400
	s_mov_b64 s[12:13], 0
	s_mov_b32 s19, 0xff5f8000
	s_movk_i32 s21, 0xa7f
	v_mov_b32_e32 v85, v69
	s_branch .LBB0_88
